# v94: v93 + M3 retention score loop back-edge test on the scalar unit and accumulators zeroed with 64-bit moves
# baseline (speedup 1.0000x reference)
.LBB0_555:
	s_and_b32 s33, s3, 1
	s_lshl_b32 s4, s33, 1
	s_add_i32 s14, s4, s18
	s_mul_i32 s4, s10, 0x1100
	s_lshl_b32 s5, s11, 7
	s_add_i32 s45, s4, s5
	s_lshl_b32 s22, s14, 6
	v_or_b32_e32 v2, s45, v116
	v_mov_b64_e32 v[50:51], s[88:89]
	s_mul_i32 s5, s14, 0x44
	s_ashr_i32 s23, s22, 31
	v_mad_i64_i32 v[2:3], s[14:15], v2, s60, v[50:51]
	s_lshl_b64 s[14:15], s[22:23], 1
	v_mov_b32_e32 v101, v0
	v_lshl_add_u64 v[2:3], v[2:3], 0, s[14:15]
	v_or_b32_e32 v10, s45, v117
	v_lshl_add_u64 v[2:3], v[2:3], 0, v[100:101]
	v_mad_i64_i32 v[10:11], s[26:27], v10, s60, v[50:51]
	s_mul_i32 s4, s10, 0x110
	v_add_co_u32_e32 v6, vcc, s78, v2
	v_lshl_add_u64 v[10:11], v[10:11], 0, s[14:15]
	v_or_b32_e32 v18, s45, v118
	s_add_i32 s4, s4, s5
	v_addc_co_u32_e32 v7, vcc, 0, v3, vcc
	v_lshl_add_u64 v[10:11], v[10:11], 0, v[100:101]
	v_mad_i64_i32 v[18:19], s[26:27], v18, s60, v[50:51]
	s_add_i32 s4, s4, s11
	v_add_co_u32_e32 v14, vcc, s78, v10
	v_lshl_add_u64 v[18:19], v[18:19], 0, s[14:15]
	v_or_b32_e32 v26, s45, v119
	s_ashr_i32 s5, s4, 31
	v_addc_co_u32_e32 v15, vcc, 0, v11, vcc
	v_lshl_add_u64 v[18:19], v[18:19], 0, v[100:101]
	v_mad_i64_i32 v[26:27], s[26:27], v26, s60, v[50:51]
	s_lshl_b64 s[10:11], s[4:5], 13
	s_add_i32 s4, s4, 34
	v_add_co_u32_e32 v22, vcc, s78, v18
	v_lshl_add_u64 v[26:27], v[26:27], 0, s[14:15]
	s_ashr_i32 s5, s4, 31
	v_addc_co_u32_e32 v23, vcc, 0, v19, vcc
	v_lshl_add_u64 v[26:27], v[26:27], 0, v[100:101]
	s_lshl_b64 s[4:5], s[4:5], 13
	v_add_co_u32_e32 v30, vcc, s78, v26
	s_cmp_eq_u32 s33, 0
	s_nop 0
	v_addc_co_u32_e32 v31, vcc, 0, v27, vcc
	s_cselect_b64 vcc, -1, 0
	s_add_u32 s10, s66, s10
	s_addc_u32 s11, s67, s11
	s_add_u32 s4, s66, s4
	s_addc_u32 s5, s67, s5
	v_or_b32_e32 v104, s45, v109
	global_load_dwordx4 v[2:5], v[6:7], off offset:512
	s_nop 0
	global_load_dwordx4 v[6:9], v[6:7], off
	s_nop 0
	global_load_dwordx4 v[10:13], v[14:15], off offset:512
	s_nop 0
	global_load_dwordx4 v[14:17], v[14:15], off
	s_nop 0
	global_load_dwordx4 v[18:21], v[22:23], off offset:512
	s_nop 0
	global_load_dwordx4 v[22:25], v[22:23], off
	s_nop 0
	global_load_dwordx4 v[26:29], v[30:31], off offset:512
	s_nop 0
	global_load_dwordx4 v[30:33], v[30:31], off
	s_nop 0
	global_load_dwordx4 v[34:37], v125, s[10:11]
	global_load_dwordx4 v[38:41], v125, s[4:5]
	global_load_dwordx4 v[42:45], v126, s[10:11]
	global_load_dwordx4 v[46:49], v126, s[4:5]
	v_mad_i64_i32 v[106:107], s[4:5], v104, s60, v[50:51]
	v_lshl_add_u64 v[50:51], v[106:107], 0, s[14:15]
	v_mov_b32_e32 v103, v0
	v_lshl_add_u64 v[50:51], v[50:51], 0, v[102:103]
	global_load_dwordx4 v[78:81], v[50:51], off offset:3584
	global_load_dwordx4 v[74:77], v[50:51], off offset:3616
	global_load_dwordx4 v[70:73], v[50:51], off offset:3648
	global_load_dwordx4 v[66:69], v[50:51], off offset:3680
	v_cndmask_b32_e32 v50, v142, v1, vcc
	s_mov_b32 s10, 0
	v_mul_f32_e32 v101, 0xbfb8aa3b, v50
	v_ashrrev_i32_e32 v105, 31, v104
	s_mov_b64 s[4:5], -1
	s_waitcnt vmcnt(15)
	ds_write_b128 v127, v[2:5]
	s_waitcnt vmcnt(14)
	ds_write_b128 v128, v[6:9] offset:16384
	s_waitcnt vmcnt(13)
	ds_write_b128 v129, v[10:13]
	s_waitcnt vmcnt(12)
	ds_write_b128 v130, v[14:17] offset:16384
	s_waitcnt vmcnt(11)
	ds_write_b128 v127, v[18:21] offset:8192
	s_waitcnt vmcnt(10)
	ds_write_b128 v131, v[22:25] offset:16384
	s_waitcnt vmcnt(9)
	ds_write_b128 v132, v[26:29] offset:8192
	s_waitcnt vmcnt(8)
	ds_write_b128 v133, v[30:33] offset:16384
	s_waitcnt vmcnt(7)
	ds_write_b128 v128, v[34:37] offset:32768
	s_waitcnt vmcnt(6)
	ds_write_b128 v128, v[38:41] offset:40960
	s_waitcnt vmcnt(5)
	ds_write_b128 v130, v[42:45] offset:32768
	s_waitcnt vmcnt(4)
	ds_write_b128 v130, v[46:49] offset:40960
	v_cndmask_b32_e32 v2, v143, v141, vcc
	v_mul_f32_e32 v103, 0xbfb8aa3b, v2
	v_mul_f32_e32 v167, 0xbf800000, v101
	v_mul_f32_e32 v168, 0xc0000000, v101
	v_mul_f32_e32 v169, 0xc0400000, v101
	v_mul_f32_e32 v170, 0xc1000000, v101
	v_mul_f32_e32 v171, 0x3f800000, v103
	v_mul_f32_e32 v172, 0x40000000, v103
	v_mul_f32_e32 v173, 0x40400000, v103
	v_mul_f32_e32 v174, 0x41000000, v103
	v_exp_f32_e32 v167, v167
	v_exp_f32_e32 v168, v168
	v_exp_f32_e32 v169, v169
	v_exp_f32_e32 v170, v170
	v_exp_f32_e32 v171, v171
	v_exp_f32_e32 v172, v172
	v_exp_f32_e32 v173, v173
	v_exp_f32_e32 v174, v174
	v_mov_b64_e32 v[2:3], 0
	v_mov_b64_e32 v[4:5], 0
	v_mov_b64_e32 v[6:7], 0
	v_mov_b64_e32 v[8:9], 0
	v_mov_b64_e32 v[10:11], 0
	v_mov_b64_e32 v[12:13], 0
	v_mov_b64_e32 v[14:15], 0
	v_mov_b64_e32 v[16:17], 0
	v_mov_b64_e32 v[18:19], 0
	v_mov_b64_e32 v[20:21], 0
	v_mov_b64_e32 v[22:23], 0
	v_mov_b64_e32 v[24:25], 0
	v_mov_b64_e32 v[26:27], 0
	v_mov_b64_e32 v[28:29], 0
	v_mov_b64_e32 v[30:31], 0
	v_mov_b64_e32 v[32:33], 0
	s_waitcnt lgkmcnt(0)
	s_barrier
	v_lshl_add_u64 v[152:153], s[22:23], 1, v[106:107]
	v_lshlrev_b32_e32 v154, 1, v82
	v_mov_b32_e32 v155, v0
	v_lshl_add_u64 v[152:153], v[152:153], 0, v[154:155]
	s_mov_b64 s[98:99], 0x1400
	v_lshl_add_u64 v[154:155], v[152:153], 0, s[98:99]
	v_add_co_u32_e32 v152, vcc, s78, v152
	s_nop 1
	v_addc_co_u32_e32 v153, vcc, 0, v153, vcc
	global_load_dwordx2 v[222:223], v[152:153], off offset:1024
	global_load_dwordx2 v[224:225], v[154:155], off offset:16
	global_load_dwordx2 v[226:227], v[154:155], off offset:32
	global_load_dwordx2 v[228:229], v[154:155], off offset:48
	global_load_dwordx2 v[230:231], v[154:155], off offset:64
	global_load_dwordx2 v[232:233], v[154:155], off offset:80
	global_load_dwordx2 v[234:235], v[154:155], off offset:96
	global_load_dwordx2 v[236:237], v[154:155], off offset:112
	v_cmp_eq_u32_e32 vcc, s22, v254
	s_cbranch_vccnz .Lm3r_wcached
	ds_read_b64 v[156:157], v0 offset:640
	s_lshl_b64 s[98:99], s[24:25], 2
	s_lshl_b64 s[100:101], s[22:23], 2
	s_add_u32 s98, s98, s100
	s_addc_u32 s99, s99, s101
	s_waitcnt lgkmcnt(0)
	v_readfirstlane_b32 s100, v156
	v_readfirstlane_b32 s101, v157
	v_lshlrev_b32_e32 v152, 2, v82
	s_add_u32 s98, s100, s98
	s_addc_u32 s99, s101, s99
	global_load_dwordx4 v[238:241], v152, s[98:99]
	global_load_dwordx4 v[242:245], v152, s[98:99] offset:32
	global_load_dwordx4 v[246:249], v152, s[98:99] offset:64
	global_load_dwordx4 v[250:253], v152, s[98:99] offset:96
	global_load_dwordx4 v[200:203], v152, s[98:99] offset:128
	global_load_dwordx4 v[204:207], v152, s[98:99] offset:160
	global_load_dwordx4 v[214:217], v152, s[98:99] offset:192
	global_load_dwordx4 v[192:195], v152, s[98:99] offset:224
	v_mov_b32_e32 v254, s22
.Lm3r_wcached:
.LBB0_556:
	s_andn2_b64 vcc, exec, s[4:5]
	s_lshl_b32 s4, s10, 6
	v_or_b32_e32 v34, s4, v108
	v_lshl_add_u32 v152, v34, 7, s58
	v_add_u32_e32 v38, v152, v120
	ds_read_b128 v[34:37], v38 offset:16384
	ds_read_b128 v[50:53], v38 offset:20480
	v_add_u32_e32 v148, v152, v121
	s_waitcnt vmcnt(11) lgkmcnt(1)
	v_mfma_f32_32x32x16_bf16 v[34:49], v[34:37], v[78:81], 0
	ds_read_b128 v[144:147], v148 offset:16384
	ds_read_b128 v[148:151], v148 offset:20480
	s_waitcnt lgkmcnt(2)
	v_mfma_f32_32x32x16_bf16 v[50:65], v[50:53], v[78:81], 0
	s_waitcnt vmcnt(10) lgkmcnt(1)
	v_mfma_f32_32x32x16_bf16 v[34:49], v[144:147], v[74:77], v[34:49]
	s_waitcnt lgkmcnt(0)
	v_mfma_f32_32x32x16_bf16 v[50:65], v[148:151], v[74:77], v[50:65]
	v_add_u32_e32 v148, v152, v122
	ds_read_b128 v[144:147], v148 offset:16384
	ds_read_b128 v[148:151], v148 offset:20480
	s_waitcnt vmcnt(9) lgkmcnt(1)
	v_mfma_f32_32x32x16_bf16 v[34:49], v[144:147], v[70:73], v[34:49]
	s_waitcnt lgkmcnt(0)
	v_mfma_f32_32x32x16_bf16 v[50:65], v[148:151], v[70:73], v[50:65]
	v_add_u32_e32 v148, v152, v123
	ds_read_b128 v[144:147], v148 offset:16384
	ds_read_b128 v[148:151], v148 offset:20480
	s_waitcnt vmcnt(8) lgkmcnt(1)
	v_mfma_f32_32x32x16_bf16 v[34:49], v[144:147], v[66:69], v[34:49]
	v_or_b32_e32 v145, s4, v82
	s_waitcnt lgkmcnt(0)
	v_mfma_f32_32x32x16_bf16 v[50:65], v[148:151], v[66:69], v[50:65]
	v_sub_u32_e32 v166, v109, v145
	v_cvt_f32_i32_e32 v166, v166
	v_mul_f32_e32 v175, v101, v166
	v_mul_f32_e64 v183, -v103, v166
	v_exp_f32_e32 v175, v175
	v_exp_f32_e32 v183, v183
	s_nop 0
	v_mul_f32_e32 v176, v175, v170
	v_mul_f32_e32 v184, v183, v174
	v_mul_f32_e32 v177, v176, v170
	v_mul_f32_e32 v185, v184, v174
	v_mul_f32_e32 v178, v177, v170
	v_mul_f32_e32 v186, v185, v174
	v_mul_f32_e32 v179, v178, v170
	v_mul_f32_e32 v187, v186, v174
	v_mul_f32_e32 v180, v179, v170
	v_mul_f32_e32 v188, v187, v174
	v_mul_f32_e32 v181, v180, v170
	v_mul_f32_e32 v189, v188, v174
	v_mul_f32_e32 v182, v181, v170
	v_mul_f32_e32 v190, v189, v174
	v_min_f32_e32 v160, v175, v183
	v_mul_f32_e32 v144, v34, v160
	v_min_f32_e32 v162, v179, v187
	v_mul_f32_e32 v34, v50, v162
	v_mul_f32_e32 v164, v175, v167
	v_mul_f32_e32 v165, v183, v171
	v_min_f32_e32 v164, v164, v165
	v_mul_f32_e32 v50, v35, v164
	v_mul_f32_e32 v160, v179, v167
	v_mul_f32_e32 v161, v187, v171
	v_min_f32_e32 v160, v160, v161
	v_mul_f32_e32 v35, v51, v160
	v_mul_f32_e32 v162, v175, v168
	v_mul_f32_e32 v163, v183, v172
	v_min_f32_e32 v162, v162, v163
	v_mul_f32_e32 v51, v36, v162
	v_mul_f32_e32 v164, v179, v168
	v_mul_f32_e32 v165, v187, v172
	v_min_f32_e32 v164, v164, v165
	v_mul_f32_e32 v36, v52, v164
	v_mul_f32_e32 v160, v175, v169
	v_mul_f32_e32 v161, v183, v173
	v_min_f32_e32 v160, v160, v161
	v_mul_f32_e32 v52, v37, v160
	v_mul_f32_e32 v162, v179, v169
	v_mul_f32_e32 v163, v187, v173
	v_min_f32_e32 v162, v162, v163
	v_mul_f32_e32 v37, v53, v162
	v_min_f32_e32 v164, v176, v184
	v_mul_f32_e32 v53, v38, v164
	v_min_f32_e32 v160, v180, v188
	v_mul_f32_e32 v38, v54, v160
	v_mul_f32_e32 v162, v176, v167
	v_mul_f32_e32 v163, v184, v171
	v_min_f32_e32 v162, v162, v163
	v_mul_f32_e32 v54, v39, v162
	v_mul_f32_e32 v164, v180, v167
	v_mul_f32_e32 v165, v188, v171
	v_min_f32_e32 v164, v164, v165
	v_mul_f32_e32 v39, v55, v164
	v_mul_f32_e32 v160, v176, v168
	v_mul_f32_e32 v161, v184, v172
	v_min_f32_e32 v160, v160, v161
	v_mul_f32_e32 v55, v40, v160
	v_mul_f32_e32 v162, v180, v168
	v_mul_f32_e32 v163, v188, v172
	v_min_f32_e32 v162, v162, v163
	v_mul_f32_e32 v40, v56, v162
	v_mul_f32_e32 v164, v176, v169
	v_mul_f32_e32 v165, v184, v173
	v_min_f32_e32 v164, v164, v165
	v_mul_f32_e32 v56, v41, v164
	v_mul_f32_e32 v160, v180, v169
	v_mul_f32_e32 v161, v188, v173
	v_min_f32_e32 v160, v160, v161
	v_mul_f32_e32 v41, v57, v160
	v_min_f32_e32 v162, v177, v185
	v_mul_f32_e32 v57, v42, v162
	v_min_f32_e32 v164, v181, v189
	v_mul_f32_e32 v42, v58, v164
	v_mul_f32_e32 v160, v177, v167
	v_mul_f32_e32 v161, v185, v171
	v_min_f32_e32 v160, v160, v161
	v_mul_f32_e32 v43, v43, v160
	v_mul_f32_e32 v162, v181, v167
	v_mul_f32_e32 v163, v189, v171
	v_min_f32_e32 v162, v162, v163
	v_mul_f32_e32 v58, v59, v162
	v_mul_f32_e32 v164, v177, v168
	v_mul_f32_e32 v165, v185, v172
	v_min_f32_e32 v164, v164, v165
	v_mul_f32_e32 v59, v44, v164
	v_mul_f32_e32 v160, v181, v168
	v_mul_f32_e32 v161, v189, v172
	v_min_f32_e32 v160, v160, v161
	v_mul_f32_e32 v60, v60, v160
	v_mul_f32_e32 v162, v177, v169
	v_mul_f32_e32 v163, v185, v173
	v_min_f32_e32 v162, v162, v163
	v_mul_f32_e32 v147, v45, v162
	v_mul_f32_e32 v164, v181, v169
	v_mul_f32_e32 v165, v189, v173
	v_min_f32_e32 v164, v164, v165
	v_mul_f32_e32 v61, v61, v164
	v_min_f32_e32 v160, v178, v186
	v_mul_f32_e32 v146, v46, v160
	v_min_f32_e32 v162, v182, v190
	v_mul_f32_e32 v62, v62, v162
	v_mul_f32_e32 v164, v178, v167
	v_mul_f32_e32 v165, v186, v171
	v_min_f32_e32 v164, v164, v165
	v_mul_f32_e32 v148, v47, v164
	v_mul_f32_e32 v160, v182, v167
	v_mul_f32_e32 v161, v190, v171
	v_min_f32_e32 v160, v160, v161
	v_mul_f32_e32 v63, v63, v160
	v_mul_f32_e32 v162, v178, v168
	v_mul_f32_e32 v163, v186, v172
	v_min_f32_e32 v162, v162, v163
	v_mul_f32_e32 v149, v48, v162
	v_mul_f32_e32 v164, v182, v168
	v_mul_f32_e32 v165, v190, v172
	v_min_f32_e32 v164, v164, v165
	v_mul_f32_e32 v64, v64, v164
	v_mul_f32_e32 v160, v178, v169
	v_mul_f32_e32 v161, v186, v173
	v_min_f32_e32 v160, v160, v161
	v_mul_f32_e32 v145, v49, v160
	v_mul_f32_e32 v162, v182, v169
	v_mul_f32_e32 v163, v190, v173
	v_min_f32_e32 v162, v162, v163
	v_mul_f32_e32 v65, v65, v162
	v_cvt_pk_bf16_f32 v44, v144, v50
	v_cvt_pk_bf16_f32 v45, v51, v52
	v_cvt_pk_bf16_f32 v46, v53, v54
	v_cvt_pk_bf16_f32 v47, v55, v56
	v_cvt_pk_bf16_f32 v48, v57, v43
	v_cvt_pk_bf16_f32 v49, v59, v147
	v_cvt_pk_bf16_f32 v50, v146, v148
	v_cvt_pk_bf16_f32 v51, v149, v145
	v_cvt_pk_bf16_f32 v34, v34, v35
	v_cvt_pk_bf16_f32 v35, v36, v37
	v_cvt_pk_bf16_f32 v36, v38, v39
	v_cvt_pk_bf16_f32 v37, v40, v41
	v_cvt_pk_bf16_f32 v38, v42, v58
	v_cvt_pk_bf16_f32 v39, v60, v61
	v_cvt_pk_bf16_f32 v40, v62, v63
	v_cvt_pk_bf16_f32 v41, v64, v65
	v_lshl_add_u32 v42, s10, 13, v110
	ds_read_b64_tr_b16 v[52:53], v42 offset:0
	ds_read_b64_tr_b16 v[54:55], v42 offset:0x400
	ds_read_b64_tr_b16 v[56:57], v42 offset:0x800
	ds_read_b64_tr_b16 v[58:59], v42 offset:0xc00
	ds_read_b64_tr_b16 v[60:61], v42 offset:0x1000
	ds_read_b64_tr_b16 v[62:63], v42 offset:0x1400
	ds_read_b64_tr_b16 v[144:145], v42 offset:0x1800
	ds_read_b64_tr_b16 v[146:147], v42 offset:0x1c00
	s_waitcnt lgkmcnt(0)
	v_permlane32_swap_b32_e32 v44, v46
	v_permlane32_swap_b32_e32 v45, v47
	v_permlane32_swap_b32_e32 v48, v50
	v_permlane32_swap_b32_e32 v49, v51
	v_permlane32_swap_b32_e32 v34, v36
	v_permlane32_swap_b32_e32 v35, v37
	v_permlane32_swap_b32_e32 v38, v40
	v_permlane32_swap_b32_e32 v39, v41
	v_mfma_f32_32x32x16_bf16 v[18:33], v[52:55], v[44:47], v[18:33]
	ds_read_b64_tr_b16 v[52:53], v42 offset:0x200
	ds_read_b64_tr_b16 v[54:55], v42 offset:0x600
	v_mfma_f32_32x32x16_bf16 v[18:33], v[56:59], v[48:51], v[18:33]
	ds_read_b64_tr_b16 v[56:57], v42 offset:0xa00
	ds_read_b64_tr_b16 v[58:59], v42 offset:0xe00
	v_mfma_f32_32x32x16_bf16 v[18:33], v[60:63], v[34:37], v[18:33]
	ds_read_b64_tr_b16 v[60:61], v42 offset:0x1200
	ds_read_b64_tr_b16 v[62:63], v42 offset:0x1600
	v_mfma_f32_32x32x16_bf16 v[18:33], v[144:147], v[38:41], v[18:33]
	ds_read_b64_tr_b16 v[144:145], v42 offset:0x1a00
	ds_read_b64_tr_b16 v[146:147], v42 offset:0x1e00
	s_waitcnt lgkmcnt(0)
	v_mfma_f32_32x32x16_bf16 v[2:17], v[52:55], v[44:47], v[2:17]
	s_mov_b64 s[4:5], 0
	s_and_b64 vcc, exec, vcc
	s_mov_b32 s10, 1
	v_mfma_f32_32x32x16_bf16 v[2:17], v[56:59], v[48:51], v[2:17]
	v_mfma_f32_32x32x16_bf16 v[2:17], v[60:63], v[34:37], v[2:17]
	v_mfma_f32_32x32x16_bf16 v[2:17], v[144:147], v[38:41], v[2:17]
	s_cbranch_vccz .LBB0_556
	v_mul_f32_e32 v34, v101, v111
	v_exp_f32_e32 v50, v34
	v_mul_f32_e32 v34, v103, v112
	v_exp_f32_e32 v51, v34
	v_lshlrev_b32_e32 v35, 16, v78
	v_and_b32_e32 v36, 0xffff0000, v78
	v_mul_f32_e32 v34, v50, v35
	v_mul_f32_e32 v37, v50, v36
	v_mul_f32_e32 v36, v51, v36
	v_cvt_pk_bf16_f32 v34, v34, v37
	v_mul_f32_e32 v35, v51, v35
	v_cvt_pk_bf16_f32 v38, v35, v36
	v_lshlrev_b32_e32 v36, 16, v79
	v_and_b32_e32 v37, 0xffff0000, v79
	v_mul_f32_e32 v35, v50, v36
	v_mul_f32_e32 v39, v50, v37
	v_mul_f32_e32 v37, v51, v37
	v_cvt_pk_bf16_f32 v35, v35, v39
	v_mul_f32_e32 v36, v51, v36
	v_cvt_pk_bf16_f32 v39, v36, v37
	v_lshlrev_b32_e32 v37, 16, v80
	v_and_b32_e32 v40, 0xffff0000, v80
	v_mul_f32_e32 v36, v50, v37
	v_mul_f32_e32 v41, v50, v40
	v_cvt_pk_bf16_f32 v36, v36, v41
	v_mul_f32_e32 v37, v51, v37
	v_mul_f32_e32 v40, v51, v40
	v_lshlrev_b32_e32 v41, 16, v81
	v_and_b32_e32 v42, 0xffff0000, v81
	v_cvt_pk_bf16_f32 v40, v37, v40
	v_mul_f32_e32 v37, v50, v41
	v_mul_f32_e32 v43, v50, v42
	v_mul_f32_e32 v41, v51, v41
	v_mul_f32_e32 v42, v51, v42
	v_cvt_pk_bf16_f32 v37, v37, v43
	v_cvt_pk_bf16_f32 v41, v41, v42
	ds_read_b128 v[42:45], v134 offset:32768
	ds_read_b128 v[46:49], v134 offset:40960
	s_waitcnt lgkmcnt(1)
	v_mfma_f32_32x32x16_bf16 v[18:33], v[42:45], v[34:37], v[18:33]
	s_mov_b64 s[4:5], 0x1400
	s_waitcnt lgkmcnt(0)
	v_mfma_f32_32x32x16_bf16 v[18:33], v[46:49], v[38:41], v[18:33]
	ds_read_b128 v[42:45], v134 offset:36864
	ds_read_b128 v[46:49], v134 offset:45056
	s_waitcnt lgkmcnt(1)
	v_mfma_f32_32x32x16_bf16 v[2:17], v[42:45], v[34:37], v[2:17]
	v_lshlrev_b32_e32 v35, 16, v74
	v_and_b32_e32 v36, 0xffff0000, v74
	v_mul_f32_e32 v34, v50, v35
	v_mul_f32_e32 v37, v50, v36
	v_mul_f32_e32 v36, v51, v36
	v_cvt_pk_bf16_f32 v34, v34, v37
	v_mul_f32_e32 v35, v51, v35
	s_waitcnt lgkmcnt(0)
	v_mfma_f32_32x32x16_bf16 v[2:17], v[46:49], v[38:41], v[2:17]
	v_cvt_pk_bf16_f32 v38, v35, v36
	v_lshlrev_b32_e32 v36, 16, v75
	v_and_b32_e32 v37, 0xffff0000, v75
	v_mul_f32_e32 v35, v50, v36
	v_mul_f32_e32 v39, v50, v37
	v_mul_f32_e32 v37, v51, v37
	v_cvt_pk_bf16_f32 v35, v35, v39
	v_mul_f32_e32 v36, v51, v36
	v_cvt_pk_bf16_f32 v39, v36, v37
	v_lshlrev_b32_e32 v37, 16, v76
	v_and_b32_e32 v40, 0xffff0000, v76
	v_mul_f32_e32 v36, v50, v37
	v_mul_f32_e32 v41, v50, v40
	v_cvt_pk_bf16_f32 v36, v36, v41
	v_mul_f32_e32 v37, v51, v37
	v_mul_f32_e32 v40, v51, v40
	v_lshlrev_b32_e32 v41, 16, v77
	v_and_b32_e32 v42, 0xffff0000, v77
	v_cvt_pk_bf16_f32 v40, v37, v40
	v_mul_f32_e32 v37, v50, v41
	v_mul_f32_e32 v43, v50, v42
	v_mul_f32_e32 v41, v51, v41
	v_mul_f32_e32 v42, v51, v42
	v_cvt_pk_bf16_f32 v37, v37, v43
	v_cvt_pk_bf16_f32 v41, v41, v42
	ds_read_b128 v[42:45], v135 offset:32768
	ds_read_b128 v[46:49], v135 offset:40960
	s_waitcnt lgkmcnt(1)
	v_mfma_f32_32x32x16_bf16 v[18:33], v[42:45], v[34:37], v[18:33]
	s_waitcnt lgkmcnt(0)
	v_mfma_f32_32x32x16_bf16 v[18:33], v[46:49], v[38:41], v[18:33]
	ds_read_b128 v[42:45], v135 offset:36864
	ds_read_b128 v[46:49], v135 offset:45056
	s_waitcnt lgkmcnt(1)
	v_mfma_f32_32x32x16_bf16 v[2:17], v[42:45], v[34:37], v[2:17]
	v_lshlrev_b32_e32 v35, 16, v70
	v_and_b32_e32 v36, 0xffff0000, v70
	v_mul_f32_e32 v34, v50, v35
	v_mul_f32_e32 v37, v50, v36
	v_mul_f32_e32 v36, v51, v36
	v_cvt_pk_bf16_f32 v34, v34, v37
	v_mul_f32_e32 v35, v51, v35
	s_waitcnt lgkmcnt(0)
	v_mfma_f32_32x32x16_bf16 v[2:17], v[46:49], v[38:41], v[2:17]
	v_cvt_pk_bf16_f32 v38, v35, v36
	v_lshlrev_b32_e32 v36, 16, v71
	v_and_b32_e32 v37, 0xffff0000, v71
	v_mul_f32_e32 v35, v50, v36
	v_mul_f32_e32 v39, v50, v37
	v_mul_f32_e32 v37, v51, v37
	v_cvt_pk_bf16_f32 v35, v35, v39
	v_mul_f32_e32 v36, v51, v36
	v_cvt_pk_bf16_f32 v39, v36, v37
	v_lshlrev_b32_e32 v37, 16, v72
	v_and_b32_e32 v40, 0xffff0000, v72
	v_mul_f32_e32 v36, v50, v37
	v_mul_f32_e32 v41, v50, v40
	v_cvt_pk_bf16_f32 v36, v36, v41
	v_mul_f32_e32 v37, v51, v37
	v_mul_f32_e32 v40, v51, v40
	v_lshlrev_b32_e32 v41, 16, v73
	v_and_b32_e32 v42, 0xffff0000, v73
	v_cvt_pk_bf16_f32 v40, v37, v40
	v_mul_f32_e32 v37, v50, v41
	v_mul_f32_e32 v43, v50, v42
	v_mul_f32_e32 v41, v51, v41
	v_mul_f32_e32 v42, v51, v42
	v_cvt_pk_bf16_f32 v37, v37, v43
	v_cvt_pk_bf16_f32 v41, v41, v42
	ds_read_b128 v[42:45], v136 offset:32768
	ds_read_b128 v[46:49], v136 offset:40960
	s_waitcnt lgkmcnt(1)
	v_mfma_f32_32x32x16_bf16 v[18:33], v[42:45], v[34:37], v[18:33]
	s_waitcnt lgkmcnt(0)
	v_mfma_f32_32x32x16_bf16 v[18:33], v[46:49], v[38:41], v[18:33]
	ds_read_b128 v[42:45], v136 offset:36864
	ds_read_b128 v[46:49], v136 offset:45056
	s_waitcnt lgkmcnt(1)
	v_mfma_f32_32x32x16_bf16 v[2:17], v[42:45], v[34:37], v[2:17]
	v_lshlrev_b32_e32 v35, 16, v66
	v_and_b32_e32 v36, 0xffff0000, v66
	v_mul_f32_e32 v34, v50, v35
	v_mul_f32_e32 v37, v50, v36
	v_mul_f32_e32 v36, v51, v36
	v_cvt_pk_bf16_f32 v34, v34, v37
	v_mul_f32_e32 v35, v51, v35
	s_waitcnt lgkmcnt(0)
	v_mfma_f32_32x32x16_bf16 v[2:17], v[46:49], v[38:41], v[2:17]
	v_cvt_pk_bf16_f32 v38, v35, v36
	v_lshlrev_b32_e32 v36, 16, v67
	v_and_b32_e32 v37, 0xffff0000, v67
	v_mul_f32_e32 v35, v50, v36
	v_mul_f32_e32 v39, v50, v37
	v_mul_f32_e32 v37, v51, v37
	v_cvt_pk_bf16_f32 v35, v35, v39
	v_mul_f32_e32 v36, v51, v36
	v_cvt_pk_bf16_f32 v39, v36, v37
	v_lshlrev_b32_e32 v37, 16, v68
	v_and_b32_e32 v40, 0xffff0000, v68
	v_mul_f32_e32 v36, v50, v37
	v_mul_f32_e32 v41, v50, v40
	v_cvt_pk_bf16_f32 v36, v36, v41
	v_mul_f32_e32 v37, v51, v37
	v_mul_f32_e32 v40, v51, v40
	v_lshlrev_b32_e32 v41, 16, v69
	v_and_b32_e32 v42, 0xffff0000, v69
	v_cvt_pk_bf16_f32 v40, v37, v40
	v_mul_f32_e32 v37, v50, v41
	v_mul_f32_e32 v43, v50, v42
	v_mul_f32_e32 v41, v51, v41
	v_mul_f32_e32 v42, v51, v42
	v_cvt_pk_bf16_f32 v37, v37, v43
	v_cvt_pk_bf16_f32 v41, v41, v42
	ds_read_b128 v[42:45], v137 offset:32768
	ds_read_b128 v[46:49], v137 offset:40960
	s_waitcnt lgkmcnt(1)
	v_mfma_f32_32x32x16_bf16 v[18:33], v[42:45], v[34:37], v[18:33]
	s_waitcnt lgkmcnt(0)
	v_mfma_f32_32x32x16_bf16 v[18:33], v[46:49], v[38:41], v[18:33]
	ds_read_b128 v[42:45], v137 offset:36864
	ds_read_b128 v[46:49], v137 offset:45056
	s_waitcnt lgkmcnt(1)
	v_mfma_f32_32x32x16_bf16 v[2:17], v[42:45], v[34:37], v[2:17]
	s_waitcnt lgkmcnt(0)
	v_mfma_f32_32x32x16_bf16 v[2:17], v[46:49], v[38:41], v[2:17]
	s_nop 7
	v_mul_f32_e32 v78, v19, v19
	v_fmac_f32_e32 v78, v18, v18
	v_fmac_f32_e32 v78, v20, v20
	v_fmac_f32_e32 v78, v21, v21
	v_fmac_f32_e32 v78, v22, v22
	v_fmac_f32_e32 v78, v23, v23
	v_fmac_f32_e32 v78, v24, v24
	v_fmac_f32_e32 v78, v25, v25
	v_fmac_f32_e32 v78, v26, v26
	v_fmac_f32_e32 v78, v27, v27
	v_fmac_f32_e32 v78, v28, v28
	v_fmac_f32_e32 v78, v29, v29
	v_fmac_f32_e32 v78, v30, v30
	v_fmac_f32_e32 v78, v31, v31
	v_fmac_f32_e32 v78, v32, v32
	v_fmac_f32_e32 v78, v33, v33
	v_fmac_f32_e32 v78, v2, v2
	v_fmac_f32_e32 v78, v3, v3
	v_fmac_f32_e32 v78, v4, v4
	v_fmac_f32_e32 v78, v5, v5
	v_fmac_f32_e32 v78, v6, v6
	v_fmac_f32_e32 v78, v7, v7
	v_fmac_f32_e32 v78, v8, v8
	v_fmac_f32_e32 v78, v9, v9
	v_fmac_f32_e32 v78, v10, v10
	v_fmac_f32_e32 v78, v11, v11
	v_fmac_f32_e32 v78, v12, v12
	v_fmac_f32_e32 v78, v13, v13
	v_fmac_f32_e32 v78, v14, v14
	v_fmac_f32_e32 v78, v15, v15
	v_pk_mul_f32 v[62:63], v[16:17], v[16:17]
	s_and_b64 vcc, exec, s[20:21]
	v_add_f32_e32 v62, v78, v62
	v_add_f32_e32 v62, v62, v63
	v_mov_b32_e32 v63, v62
	s_nop 1
	v_permlane32_swap_b32_e32 v62, v63
	v_add_f32_e32 v62, v62, v63
	v_fmamk_f32 v62, v62, 0x3c800000, v210
	v_rsq_f32_e32 v78, v62
	v_lshlrev_b64 v[62:63], 10, v[104:105]
	v_lshl_add_u64 v[62:63], s[82:83], 0, v[62:63]
	v_lshl_add_u64 v[62:63], v[62:63], 0, s[22:23]
	v_mul_f32_e32 v78, 0x41800000, v78
	v_lshl_add_u64 v[62:63], v[62:63], 0, v[84:85]
	v_rcp_f32_e32 v152, v78
	s_waitcnt vmcnt(7)
	v_lshlrev_b32_e32 v153, 16, v222
	v_and_b32_e32 v154, 0xffff0000, v222
	v_lshlrev_b32_e32 v155, 16, v223
	v_and_b32_e32 v156, 0xffff0000, v223
	v_mul_f32_e32 v157, 0xbfb8aa3b, v153
	v_mul_f32_e32 v158, 0xbfb8aa3b, v154
	v_mul_f32_e32 v159, 0xbfb8aa3b, v155
	v_mul_f32_e32 v160, 0xbfb8aa3b, v156
	v_exp_f32_e32 v157, v157
	v_exp_f32_e32 v158, v158
	v_exp_f32_e32 v159, v159
	v_exp_f32_e32 v160, v160
	v_mul_f32_e32 v161, v18, v238
	v_mul_f32_e32 v162, v19, v239
	v_mul_f32_e32 v163, v20, v240
	v_mul_f32_e32 v164, v21, v241
	v_fma_f32 v157, v157, v152, v152
	v_fma_f32 v158, v158, v152, v152
	v_fma_f32 v159, v159, v152, v152
	v_fma_f32 v160, v160, v152, v152
	v_rcp_f32_e32 v157, v157
	v_rcp_f32_e32 v158, v158
	v_rcp_f32_e32 v159, v159
	v_rcp_f32_e32 v160, v160
	v_mul_f32_e32 v153, v153, v157
	v_mul_f32_e32 v154, v154, v158
	v_mul_f32_e32 v155, v155, v159
	v_mul_f32_e32 v156, v156, v160
	v_mul_f32_e32 v161, v161, v153
	v_mul_f32_e32 v162, v162, v154
	v_mul_f32_e32 v163, v163, v155
	v_mul_f32_e32 v164, v164, v156
	v_cvt_pk_fp8_f32 v18, v161, v162
	v_cvt_pk_fp8_f32 v18, v163, v164 op_sel:[0,0,1]
	s_waitcnt vmcnt(6)
	v_lshlrev_b32_e32 v165, 16, v224
	v_and_b32_e32 v166, 0xffff0000, v224
	v_lshlrev_b32_e32 v167, 16, v225
	v_and_b32_e32 v168, 0xffff0000, v225
	v_mul_f32_e32 v169, 0xbfb8aa3b, v165
	v_mul_f32_e32 v170, 0xbfb8aa3b, v166
	v_mul_f32_e32 v171, 0xbfb8aa3b, v167
	v_mul_f32_e32 v172, 0xbfb8aa3b, v168
	v_exp_f32_e32 v169, v169
	v_exp_f32_e32 v170, v170
	v_exp_f32_e32 v171, v171
	v_exp_f32_e32 v172, v172
	v_mul_f32_e32 v173, v22, v242
	v_mul_f32_e32 v174, v23, v243
	v_mul_f32_e32 v175, v24, v244
	v_mul_f32_e32 v176, v25, v245
	v_fma_f32 v169, v169, v152, v152
	v_fma_f32 v170, v170, v152, v152
	v_fma_f32 v171, v171, v152, v152
	v_fma_f32 v172, v172, v152, v152
	v_rcp_f32_e32 v169, v169
	v_rcp_f32_e32 v170, v170
	v_rcp_f32_e32 v171, v171
	v_rcp_f32_e32 v172, v172
	v_mul_f32_e32 v165, v165, v169
	v_mul_f32_e32 v166, v166, v170
	v_mul_f32_e32 v167, v167, v171
	v_mul_f32_e32 v168, v168, v172
	v_mul_f32_e32 v173, v173, v165
	v_mul_f32_e32 v174, v174, v166
	v_mul_f32_e32 v175, v175, v167
	v_mul_f32_e32 v176, v176, v168
	v_cvt_pk_fp8_f32 v20, v173, v174
	v_cvt_pk_fp8_f32 v20, v175, v176 op_sel:[0,0,1]
	s_waitcnt vmcnt(5)
	v_lshlrev_b32_e32 v153, 16, v226
	v_and_b32_e32 v154, 0xffff0000, v226
	v_lshlrev_b32_e32 v155, 16, v227
	v_and_b32_e32 v156, 0xffff0000, v227
	v_mul_f32_e32 v157, 0xbfb8aa3b, v153
	v_mul_f32_e32 v158, 0xbfb8aa3b, v154
	v_mul_f32_e32 v159, 0xbfb8aa3b, v155
	v_mul_f32_e32 v160, 0xbfb8aa3b, v156
	v_exp_f32_e32 v157, v157
	v_exp_f32_e32 v158, v158
	v_exp_f32_e32 v159, v159
	v_exp_f32_e32 v160, v160
	v_mul_f32_e32 v161, v26, v246
	v_mul_f32_e32 v162, v27, v247
	v_mul_f32_e32 v163, v28, v248
	v_mul_f32_e32 v164, v29, v249
	v_fma_f32 v157, v157, v152, v152
	v_fma_f32 v158, v158, v152, v152
	v_fma_f32 v159, v159, v152, v152
	v_fma_f32 v160, v160, v152, v152
	v_rcp_f32_e32 v157, v157
	v_rcp_f32_e32 v158, v158
	v_rcp_f32_e32 v159, v159
	v_rcp_f32_e32 v160, v160
	v_mul_f32_e32 v153, v153, v157
	v_mul_f32_e32 v154, v154, v158
	v_mul_f32_e32 v155, v155, v159
	v_mul_f32_e32 v156, v156, v160
	v_mul_f32_e32 v161, v161, v153
	v_mul_f32_e32 v162, v162, v154
	v_mul_f32_e32 v163, v163, v155
	v_mul_f32_e32 v164, v164, v156
	v_cvt_pk_fp8_f32 v19, v161, v162
	v_cvt_pk_fp8_f32 v19, v163, v164 op_sel:[0,0,1]
	s_waitcnt vmcnt(4)
	v_lshlrev_b32_e32 v165, 16, v228
	v_and_b32_e32 v166, 0xffff0000, v228
	v_lshlrev_b32_e32 v167, 16, v229
	v_and_b32_e32 v168, 0xffff0000, v229
	v_mul_f32_e32 v169, 0xbfb8aa3b, v165
	v_mul_f32_e32 v170, 0xbfb8aa3b, v166
	v_mul_f32_e32 v171, 0xbfb8aa3b, v167
	v_mul_f32_e32 v172, 0xbfb8aa3b, v168
	v_exp_f32_e32 v169, v169
	v_exp_f32_e32 v170, v170
	v_exp_f32_e32 v171, v171
	v_exp_f32_e32 v172, v172
	v_mul_f32_e32 v173, v30, v250
	v_mul_f32_e32 v174, v31, v251
	v_mul_f32_e32 v175, v32, v252
	v_mul_f32_e32 v176, v33, v253
	v_fma_f32 v169, v169, v152, v152
	v_fma_f32 v170, v170, v152, v152
	v_fma_f32 v171, v171, v152, v152
	v_fma_f32 v172, v172, v152, v152
	v_rcp_f32_e32 v169, v169
	v_rcp_f32_e32 v170, v170
	v_rcp_f32_e32 v171, v171
	v_rcp_f32_e32 v172, v172
	v_mul_f32_e32 v165, v165, v169
	v_mul_f32_e32 v166, v166, v170
	v_mul_f32_e32 v167, v167, v171
	v_mul_f32_e32 v168, v168, v172
	v_mul_f32_e32 v173, v173, v165
	v_mul_f32_e32 v174, v174, v166
	v_mul_f32_e32 v175, v175, v167
	v_mul_f32_e32 v176, v176, v168
	v_cvt_pk_fp8_f32 v21, v173, v174
	v_cvt_pk_fp8_f32 v21, v175, v176 op_sel:[0,0,1]
	v_permlane32_swap_b32_e32 v18, v19
	s_nop 0
	v_permlane32_swap_b32_e32 v20, v21
	global_store_dwordx4 v[62:63], v[18:21], off offset:768
	s_waitcnt vmcnt(4)
	v_lshlrev_b32_e32 v153, 16, v230
	v_and_b32_e32 v154, 0xffff0000, v230
	v_lshlrev_b32_e32 v155, 16, v231
	v_and_b32_e32 v156, 0xffff0000, v231
	v_mul_f32_e32 v157, 0xbfb8aa3b, v153
	v_mul_f32_e32 v158, 0xbfb8aa3b, v154
	v_mul_f32_e32 v159, 0xbfb8aa3b, v155
	v_mul_f32_e32 v160, 0xbfb8aa3b, v156
	v_exp_f32_e32 v157, v157
	v_exp_f32_e32 v158, v158
	v_exp_f32_e32 v159, v159
	v_exp_f32_e32 v160, v160
	v_mul_f32_e32 v161, v2, v200
	v_mul_f32_e32 v162, v3, v201
	v_mul_f32_e32 v163, v4, v202
	v_mul_f32_e32 v164, v5, v203
	v_fma_f32 v157, v157, v152, v152
	v_fma_f32 v158, v158, v152, v152
	v_fma_f32 v159, v159, v152, v152
	v_fma_f32 v160, v160, v152, v152
	v_rcp_f32_e32 v157, v157
	v_rcp_f32_e32 v158, v158
	v_rcp_f32_e32 v159, v159
	v_rcp_f32_e32 v160, v160
	v_mul_f32_e32 v153, v153, v157
	v_mul_f32_e32 v154, v154, v158
	v_mul_f32_e32 v155, v155, v159
	v_mul_f32_e32 v156, v156, v160
	v_mul_f32_e32 v161, v161, v153
	v_mul_f32_e32 v162, v162, v154
	v_mul_f32_e32 v163, v163, v155
	v_mul_f32_e32 v164, v164, v156
	v_cvt_pk_fp8_f32 v2, v161, v162
	v_cvt_pk_fp8_f32 v2, v163, v164 op_sel:[0,0,1]
	s_waitcnt vmcnt(3)
	v_lshlrev_b32_e32 v165, 16, v232
	v_and_b32_e32 v166, 0xffff0000, v232
	v_lshlrev_b32_e32 v167, 16, v233
	v_and_b32_e32 v168, 0xffff0000, v233
	v_mul_f32_e32 v169, 0xbfb8aa3b, v165
	v_mul_f32_e32 v170, 0xbfb8aa3b, v166
	v_mul_f32_e32 v171, 0xbfb8aa3b, v167
	v_mul_f32_e32 v172, 0xbfb8aa3b, v168
	v_exp_f32_e32 v169, v169
	v_exp_f32_e32 v170, v170
	v_exp_f32_e32 v171, v171
	v_exp_f32_e32 v172, v172
	v_mul_f32_e32 v173, v6, v204
	v_mul_f32_e32 v174, v7, v205
	v_mul_f32_e32 v175, v8, v206
	v_mul_f32_e32 v176, v9, v207
	v_fma_f32 v169, v169, v152, v152
	v_fma_f32 v170, v170, v152, v152
	v_fma_f32 v171, v171, v152, v152
	v_fma_f32 v172, v172, v152, v152
	v_rcp_f32_e32 v169, v169
	v_rcp_f32_e32 v170, v170
	v_rcp_f32_e32 v171, v171
	v_rcp_f32_e32 v172, v172
	v_mul_f32_e32 v165, v165, v169
	v_mul_f32_e32 v166, v166, v170
	v_mul_f32_e32 v167, v167, v171
	v_mul_f32_e32 v168, v168, v172
	v_mul_f32_e32 v173, v173, v165
	v_mul_f32_e32 v174, v174, v166
	v_mul_f32_e32 v175, v175, v167
	v_mul_f32_e32 v176, v176, v168
	v_cvt_pk_fp8_f32 v4, v173, v174
	v_cvt_pk_fp8_f32 v4, v175, v176 op_sel:[0,0,1]
	s_waitcnt vmcnt(2)
	v_lshlrev_b32_e32 v153, 16, v234
	v_and_b32_e32 v154, 0xffff0000, v234
	v_lshlrev_b32_e32 v155, 16, v235
	v_and_b32_e32 v156, 0xffff0000, v235
	v_mul_f32_e32 v157, 0xbfb8aa3b, v153
	v_mul_f32_e32 v158, 0xbfb8aa3b, v154
	v_mul_f32_e32 v159, 0xbfb8aa3b, v155
	v_mul_f32_e32 v160, 0xbfb8aa3b, v156
	v_exp_f32_e32 v157, v157
	v_exp_f32_e32 v158, v158
	v_exp_f32_e32 v159, v159
	v_exp_f32_e32 v160, v160
	v_mul_f32_e32 v161, v10, v214
	v_mul_f32_e32 v162, v11, v215
	v_mul_f32_e32 v163, v12, v216
	v_mul_f32_e32 v164, v13, v217
	v_fma_f32 v157, v157, v152, v152
	v_fma_f32 v158, v158, v152, v152
	v_fma_f32 v159, v159, v152, v152
	v_fma_f32 v160, v160, v152, v152
	v_rcp_f32_e32 v157, v157
	v_rcp_f32_e32 v158, v158
	v_rcp_f32_e32 v159, v159
	v_rcp_f32_e32 v160, v160
	v_mul_f32_e32 v153, v153, v157
	v_mul_f32_e32 v154, v154, v158
	v_mul_f32_e32 v155, v155, v159
	v_mul_f32_e32 v156, v156, v160
	v_mul_f32_e32 v161, v161, v153
	v_mul_f32_e32 v162, v162, v154
	v_mul_f32_e32 v163, v163, v155
	v_mul_f32_e32 v164, v164, v156
	v_cvt_pk_fp8_f32 v3, v161, v162
	v_cvt_pk_fp8_f32 v3, v163, v164 op_sel:[0,0,1]
	s_waitcnt vmcnt(1)
	v_lshlrev_b32_e32 v165, 16, v236
	v_and_b32_e32 v166, 0xffff0000, v236
	v_lshlrev_b32_e32 v167, 16, v237
	v_and_b32_e32 v168, 0xffff0000, v237
	v_mul_f32_e32 v169, 0xbfb8aa3b, v165
	v_mul_f32_e32 v170, 0xbfb8aa3b, v166
	v_mul_f32_e32 v171, 0xbfb8aa3b, v167
	v_mul_f32_e32 v172, 0xbfb8aa3b, v168
	v_exp_f32_e32 v169, v169
	v_exp_f32_e32 v170, v170
	v_exp_f32_e32 v171, v171
	v_exp_f32_e32 v172, v172
	v_mul_f32_e32 v173, v14, v192
	v_mul_f32_e32 v174, v15, v193
	v_mul_f32_e32 v175, v16, v194
	v_mul_f32_e32 v176, v17, v195
	v_fma_f32 v169, v169, v152, v152
	v_fma_f32 v170, v170, v152, v152
	v_fma_f32 v171, v171, v152, v152
	v_fma_f32 v172, v172, v152, v152
	v_rcp_f32_e32 v169, v169
	v_rcp_f32_e32 v170, v170
	v_rcp_f32_e32 v171, v171
	v_rcp_f32_e32 v172, v172
	v_mul_f32_e32 v165, v165, v169
	v_mul_f32_e32 v166, v166, v170
	v_mul_f32_e32 v167, v167, v171
	v_mul_f32_e32 v168, v168, v172
	v_mul_f32_e32 v173, v173, v165
	v_mul_f32_e32 v174, v174, v166
	v_mul_f32_e32 v175, v175, v167
	v_mul_f32_e32 v176, v176, v168
	v_cvt_pk_fp8_f32 v5, v173, v174
	v_cvt_pk_fp8_f32 v5, v175, v176 op_sel:[0,0,1]
	v_permlane32_swap_b32_e32 v2, v3
	s_nop 0
	v_permlane32_swap_b32_e32 v4, v5
	global_store_dwordx4 v[62:63], v[2:5], off offset:800
	s_cbranch_vccz .LBB0_550
	s_waitcnt vmcnt(0)
	s_barrier
	s_and_saveexec_b64 s[4:5], s[0:1]
	s_cbranch_execz .LBB0_549
	s_mov_b64 s[10:11], exec
	v_mbcnt_lo_u32_b32 v2, s10, 0
	buffer_wbl2 sc1
	s_waitcnt vmcnt(0)
	s_waitcnt vmcnt(0)
	v_mbcnt_hi_u32_b32 v2, s11, v2
	v_cmp_eq_u32_e32 vcc, 0, v2
	s_and_b64 s[14:15], exec, vcc
	s_mov_b64 exec, s[14:15]
	s_cbranch_execz .LBB0_549
	s_bcnt1_i32_b64 s10, s[10:11]
	v_mov_b32_e32 v2, s10
	global_atomic_add v0, v2, s[84:85]
	s_branch .LBB0_549
